# baseline (speedup 1.0000x reference)
.LBB1_44:
	s_or_b64 exec, exec, s[0:1]
	s_xor_b64 s[0:1], s[2:3], -1
	v_and_b32_e32 v14, 3, v2
	v_lshl_add_u32 v98, v3, 4, v4
	s_and_saveexec_b64 s[2:3], s[0:1]
	s_xor_b64 s[0:1], exec, s[2:3]
	s_cbranch_execz .LBB1_56
	v_mov_b32_e32 v175, v0
	s_nop 0
	s_and_saveexec_b64 s[100:101], s[34:35]
	s_cbranch_execz .Lpoll_i_g2
	v_ashrrev_i32_e32 v99, 31, v98
	v_lshl_add_u64 v[252:253], v[98:99], 2, s[96:97]
	global_load_dword v254, v[252:253], off sc1

.LBB1_49:
	v_lshlrev_b32_e32 v16, 4, v175
	v_add_u32_e32 v19, 0x2000, v16
	v_ashrrev_i32_e32 v8, 31, v19
	v_lshrrev_b32_e32 v8, 22, v8
	v_mul_u32_u24_e32 v118, 0xc0, v14
	v_mov_b64_e32 v[2:3], s[42:43]
	v_add_u32_e32 v8, v19, v8
	v_mad_u64_u32 v[4:5], s[2:3], v118, s56, v[2:3]
	v_bfe_i32 v3, v175, 27, 1
	v_ashrrev_i32_e32 v8, 10, v8
	v_lshrrev_b32_e32 v3, 22, v3
	v_mul_i32_i24_e32 v9, 0x400, v8
	v_add_u32_e32 v3, v16, v3
	v_sub_u32_e32 v9, v19, v9
	v_and_b32_e32 v3, 0xfffffc00, v3
	v_lshrrev_b32_e32 v10, 4, v9
	v_ashrrev_i32_e32 v2, 31, v175
	v_sub_u32_e32 v3, v16, v3
	v_bitop3_b32 v9, v10, v9, 32 bitop3:0x6c
	v_lshrrev_b32_e32 v2, 26, v2
	v_lshrrev_b32_e32 v6, 4, v3
	v_ashrrev_i32_e32 v11, 31, v9
	v_add_u32_e32 v2, v175, v2
	v_bitop3_b32 v6, v6, v3, 32 bitop3:0x6c
	v_ashrrev_i32_e32 v3, 31, v3
	v_lshrrev_b32_e32 v11, 26, v11
	v_ashrrev_i32_e32 v2, 6, v2
	v_lshrrev_b32_e32 v3, 26, v3
	v_lshlrev_b32_e32 v10, 3, v8
	v_add_u32_e32 v11, v9, v11
	v_lshlrev_b32_e32 v7, 3, v2
	v_add_u32_e32 v3, v6, v3
	v_and_b32_e32 v10, -16, v10
	v_ashrrev_i32_e32 v12, 6, v11
	v_and_b32_e32 v7, -16, v7
	v_ashrrev_i32_e32 v3, 6, v3
	v_add_u32_e32 v18, v12, v10
	v_and_b32_e32 v10, 0xc0, v11
	v_add_u32_e32 v17, v3, v7
	v_mul_i32_i24_e32 v3, 64, v3
	v_lshlrev_b32_e32 v8, 5, v8
	v_sub_u32_e32 v9, v9, v10
	v_lshlrev_b32_e32 v2, 5, v2
	v_sub_u32_e32 v3, v6, v3
	v_readlane_b32 s4, v230, 6
	v_and_b32_e32 v8, 32, v8
	v_ashrrev_i16_sdwa v9, v1, sext(v9) dst_sel:DWORD dst_unused:UNUSED_PAD src0_sel:DWORD src1_sel:BYTE_0
	v_and_b32_e32 v2, 32, v2
	v_ashrrev_i16_sdwa v3, v1, sext(v3) dst_sel:DWORD dst_unused:UNUSED_PAD src0_sel:DWORD src1_sel:BYTE_0
	v_mad_i64_i32 v[6:7], s[2:3], v17, s56, v[4:5]
	v_add_u32_e32 v119, s4, v16
	v_add_u32_sdwa v8, v8, sext(v9) dst_sel:DWORD dst_unused:UNUSED_PAD src0_sel:DWORD src1_sel:WORD_0
	v_add_u32_sdwa v2, v2, sext(v3) dst_sel:DWORD dst_unused:UNUSED_PAD src0_sel:DWORD src1_sel:WORD_0
	v_readfirstlane_b32 s2, v119
	v_ashrrev_i32_e32 v9, 31, v8
	v_ashrrev_i32_e32 v3, 31, v2
	s_mov_b32 m0, s2
	v_mad_i64_i32 v[10:11], s[2:3], v18, s56, v[4:5]
	v_lshlrev_b64 v[4:5], 1, v[8:9]
	v_lshlrev_b64 v[2:3], 1, v[2:3]
	v_lshl_add_u64 v[8:9], v[10:11], 0, v[4:5]
	v_add_u32_e32 v10, s4, v19
	v_lshlrev_b32_e32 v174, 8, v98
	v_lshl_add_u64 v[6:7], v[6:7], 0, v[2:3]
	v_readfirstlane_b32 s2, v10
	v_mov_b64_e32 v[20:21], s[44:45]
	s_and_saveexec_b64 s[100:101], s[34:35]
	s_cbranch_execz .Lpoll_w_g2
	s_waitcnt vmcnt(0)
	v_cmp_gt_i32_e64 s[16:17], 4, v254
	s_and_b64 exec, exec, s[16:17]
	s_cbranch_execz .Lpoll_w_g2
	s_mov_b32 s14, 0
	s_mov_b64 s[10:11], 0
.Lpoll_l_g2:
	s_sleep 8
	global_load_dword v254, v[252:253], off sc1
	s_cmp_gt_u32 s14, 0xffffd
	s_cselect_b64 s[12:13], -1, 0
	s_add_i32 s14, s14, 1
	s_waitcnt vmcnt(0)
	v_cmp_lt_i32_e64 s[16:17], 3, v254
	s_or_b64 s[12:13], s[16:17], s[12:13]
	s_and_b64 s[12:13], exec, s[12:13]
	s_or_b64 s[10:11], s[12:13], s[10:11]
	s_andn2_b64 exec, exec, s[10:11]
	s_cbranch_execnz .Lpoll_l_g2
.Lpoll_w_g2:
	s_mov_b64 exec, s[100:101]
	s_barrier
	global_load_lds_dwordx4 v[6:7], off
	s_mov_b32 m0, s2
	v_mad_i64_i32 v[12:13], s[2:3], v174, s56, v[20:21]
	v_mad_i64_i32 v[10:11], s[2:3], v17, s56, v[12:13]
	v_add_u32_e32 v120, 0, v16
	global_load_lds_dwordx4 v[8:9], off
	v_readfirstlane_b32 s2, v120
	s_mov_b32 m0, s2
	v_mad_i64_i32 v[12:13], s[2:3], v18, s56, v[12:13]
	v_add_u32_e32 v122, 0x2000, v120
	v_mul_u32_u24_e32 v14, 0x24000, v14
	v_lshl_add_u64 v[10:11], v[10:11], 0, v[2:3]
	v_readfirstlane_b32 s2, v122
	v_lshlrev_b32_e32 v108, 1, v14
	global_load_lds_dwordx4 v[10:11], off
	s_mov_b32 m0, s2
	v_lshl_add_u64 v[14:15], s[42:43], 0, v[108:109]
	s_mov_b64 s[2:3], 0x24000
	v_lshl_add_u64 v[22:23], v[14:15], 0, s[2:3]
	v_readlane_b32 s4, v230, 7
	v_mad_i64_i32 v[24:25], s[2:3], v17, s56, v[22:23]
	s_nop 0
	v_add_u32_e32 v123, s4, v16
	v_lshl_add_u64 v[12:13], v[12:13], 0, v[4:5]
	v_readfirstlane_b32 s2, v123
	global_load_lds_dwordx4 v[12:13], off
	s_mov_b32 m0, s2
	v_mad_i64_i32 v[22:23], s[2:3], v18, s56, v[22:23]
	v_add_u32_e32 v19, s4, v19
	v_lshl_add_u64 v[24:25], v[24:25], 0, v[2:3]
	v_readfirstlane_b32 s2, v19
	v_or_b32_e32 v107, 0x80, v174
	global_load_lds_dwordx4 v[24:25], off
	v_lshl_add_u64 v[22:23], v[22:23], 0, v[4:5]
	s_mov_b32 m0, s2
	v_mad_i64_i32 v[20:21], s[2:3], v107, s56, v[20:21]
	global_load_lds_dwordx4 v[22:23], off
	v_mad_i64_i32 v[22:23], s[2:3], v17, s56, v[20:21]
	v_add_u32_e32 v125, 0x4000, v120
	v_add_u32_e32 v126, 0x6000, v120
	v_readfirstlane_b32 s2, v125
	s_mov_b32 m0, s2
	v_mad_i64_i32 v[20:21], s[2:3], v18, s56, v[20:21]
	v_lshl_add_u64 v[98:99], v[22:23], 0, v[2:3]
	v_readfirstlane_b32 s2, v126
	global_load_lds_dwordx4 v[98:99], off
	v_lshl_add_u64 v[100:101], v[20:21], 0, v[4:5]
	s_mov_b32 m0, s2
	v_and_b32_e32 v19, 0xffffff00, v175
	global_load_lds_dwordx4 v[100:101], off
	s_movk_i32 s2, 0x100
	v_cmp_eq_u32_e32 vcc, s2, v19
	s_and_saveexec_b64 s[2:3], vcc
	s_cbranch_execz .LBB1_51
	s_barrier
.LBB1_51:
	s_or_b64 exec, exec, s[2:3]
	v_mad_i64_i32 v[22:23], s[2:3], v17, s56, 0
	v_mad_i64_i32 v[18:19], s[2:3], v18, s56, 0
	v_mad_i64_i32 v[24:25], s[2:3], v174, s56, 0
	v_readlane_b32 s3, v230, 8
	s_mov_b64 s[4:5], 0x80
	v_lshl_add_u64 v[6:7], v[6:7], 0, s[4:5]
	v_add_u32_e32 v128, s3, v16
	v_add_u32_e32 v129, 0x2000, v128
	v_readfirstlane_b32 s2, v128
	s_mov_b32 m0, s2
	v_readfirstlane_b32 s2, v129
	v_add_u32_e32 v130, 0x8000, v120
	v_mov_b32_e32 v66, 0
	v_mov_b32_e32 v67, 0
	v_mov_b32_e32 v68, 0
	v_mov_b32_e32 v69, 0
	v_mov_b32_e32 v78, 0
	v_mov_b32_e32 v79, 0
	v_mov_b32_e32 v80, 0
	v_mov_b32_e32 v81, 0
	v_mov_b32_e32 v82, 0
	v_mov_b32_e32 v83, 0
	v_mov_b32_e32 v84, 0
	v_mov_b32_e32 v85, 0
	v_mov_b32_e32 v86, 0
	v_mov_b32_e32 v87, 0
	v_mov_b32_e32 v88, 0
	v_mov_b32_e32 v89, 0
	v_mov_b32_e32 v90, 0
	v_mov_b32_e32 v91, 0
	v_mov_b32_e32 v92, 0
	v_mov_b32_e32 v93, 0
	v_mov_b32_e32 v94, 0
	v_mov_b32_e32 v95, 0
	v_mov_b32_e32 v96, 0
	v_mov_b32_e32 v97, 0
	v_mov_b32_e32 v26, 0
	v_mov_b32_e32 v27, 0
	v_mov_b32_e32 v28, 0
	v_mov_b32_e32 v29, 0
	v_mov_b32_e32 v30, 0
	v_mov_b32_e32 v31, 0
	v_mov_b32_e32 v32, 0
	v_mov_b32_e32 v33, 0
	v_mov_b32_e32 v34, 0
	v_mov_b32_e32 v35, 0
	v_mov_b32_e32 v36, 0
	v_mov_b32_e32 v37, 0
	v_mov_b32_e32 v38, 0
	v_mov_b32_e32 v39, 0
	v_mov_b32_e32 v40, 0
	v_mov_b32_e32 v41, 0
	v_mov_b32_e32 v46, 0
	v_mov_b32_e32 v47, 0
	v_mov_b32_e32 v48, 0
	v_mov_b32_e32 v49, 0
	v_mov_b32_e32 v54, 0
	v_mov_b32_e32 v55, 0
	v_mov_b32_e32 v56, 0
	v_mov_b32_e32 v57, 0
	v_mov_b32_e32 v42, 0
	v_mov_b32_e32 v43, 0
	v_mov_b32_e32 v44, 0
	v_mov_b32_e32 v45, 0
	v_mov_b32_e32 v50, 0
	v_mov_b32_e32 v51, 0
	v_mov_b32_e32 v52, 0
	v_mov_b32_e32 v53, 0
	v_mov_b32_e32 v58, 0
	v_mov_b32_e32 v59, 0
	v_mov_b32_e32 v60, 0
	v_mov_b32_e32 v61, 0
	v_mov_b32_e32 v62, 0
	v_mov_b32_e32 v63, 0
	v_mov_b32_e32 v64, 0
	v_mov_b32_e32 v65, 0
	v_mov_b32_e32 v70, 0
	v_mov_b32_e32 v71, 0
	v_mov_b32_e32 v72, 0
	v_mov_b32_e32 v73, 0
	v_mov_b32_e32 v74, 0
	v_mov_b32_e32 v75, 0
	v_mov_b32_e32 v76, 0
	v_mov_b32_e32 v77, 0
	s_waitcnt vmcnt(4)
	s_barrier
	global_load_lds_dwordx4 v[6:7], off
	v_lshl_add_u64 v[6:7], v[8:9], 0, s[4:5]
	s_mov_b32 m0, s2
	v_readfirstlane_b32 s2, v130
	v_add_u32_e32 v131, 0xa000, v120
	global_load_lds_dwordx4 v[6:7], off
	v_lshl_add_u64 v[6:7], v[10:11], 0, s[4:5]
	s_mov_b32 m0, s2
	v_readfirstlane_b32 s2, v131
	global_load_lds_dwordx4 v[6:7], off
	v_lshl_add_u64 v[6:7], v[12:13], 0, s[4:5]
	s_mov_b32 m0, s2
	s_mov_b64 s[4:5], 0x24080
	global_load_lds_dwordx4 v[6:7], off
	v_lshl_add_u64 v[6:7], v[14:15], 0, s[4:5]
	v_readlane_b32 s4, v230, 9
	v_lshl_add_u64 v[8:9], v[6:7], 0, v[22:23]
	v_lshl_add_u64 v[8:9], v[8:9], 0, v[2:3]
	v_add_u32_e32 v132, s4, v16
	v_add_u32_e32 v133, 0x2000, v132
	v_readfirstlane_b32 s2, v132
	s_mov_b32 m0, s2
	v_lshl_add_u64 v[6:7], v[6:7], 0, v[18:19]
	v_readfirstlane_b32 s2, v133
	global_load_lds_dwordx4 v[8:9], off
	v_lshl_add_u64 v[6:7], v[6:7], 0, v[4:5]
	s_mov_b32 m0, s2
	v_and_b32_e32 v177, 15, v175
	global_load_lds_dwordx4 v[6:7], off
	v_and_b32_e32 v6, 64, v175
	v_lshlrev_b32_e32 v8, 2, v175
	v_cmp_ne_u32_e32 vcc, 0, v6
	v_and_b32_e32 v6, 48, v175
	v_lshlrev_b32_e32 v7, 6, v177
	v_and_b32_e32 v8, 32, v8
	v_bitop3_b32 v7, v7, v8, v6 bitop3:0x36
	v_readlane_b32 s2, v230, 6
	v_ashrrev_i32_e32 v10, 2, v175
	v_and_b32_e32 v180, 0xffffffe0, v10
	v_add_u32_e32 v9, s2, v7
	v_readlane_b32 s2, v230, 7
	v_add_u32_e32 v11, s3, v7
	v_add_u32_e32 v12, s4, v7
	v_add_u32_e32 v10, s2, v7
	v_add_u32_e32 v14, 0, v7
	v_lshlrev_b32_e32 v7, 6, v175
	s_movk_i32 s2, 0x3c0
	v_mul_u32_u24_e32 v20, 0x600, v118
	v_mov_b32_e32 v21, v109
	v_and_or_b32 v6, v7, s2, v6
	v_lshl_add_u64 v[2:3], v[22:23], 0, v[2:3]
	v_xad_u32 v8, v6, v8, 0
	v_lshl_add_u64 v[6:7], v[2:3], 0, v[20:21]
	v_lshl_add_u64 v[4:5], v[18:19], 0, v[4:5]
	v_lshl_add_u64 v[102:103], s[42:43], 0, v[6:7]
	v_lshl_add_u64 v[6:7], v[4:5], 0, v[20:21]
	v_lshl_add_u64 v[104:105], s[42:43], 0, v[6:7]
	v_lshl_add_u64 v[6:7], v[2:3], 0, v[24:25]
	v_lshl_add_u64 v[2:3], v[2:3], 0, v[108:109]
	v_cndmask_b32_e64 v179, 0, 48, vcc
	v_lshlrev_b32_e32 v15, 7, v180
	v_lshl_add_u64 v[114:115], s[42:43], 0, v[2:3]
	v_lshl_add_u64 v[2:3], v[4:5], 0, v[108:109]
	v_lshlrev_b32_e32 v13, 7, v179
	v_or_b32_e32 v16, 0x800, v15
	v_lshl_add_u64 v[110:111], s[44:45], 0, v[6:7]
	v_lshl_add_u64 v[6:7], v[4:5], 0, v[24:25]
	v_lshl_add_u64 v[116:117], s[42:43], 0, v[2:3]
	v_mov_b32_e32 v2, 0
	v_lshl_add_u64 v[112:113], s[44:45], 0, v[6:7]
	s_mov_b32 s4, -2
	s_mov_b64 s[2:3], 0
	v_add_u32_e32 v135, v9, v13
	v_add_u32_e32 v121, v14, v15
	v_add_u32_e32 v108, v8, v16
	v_add_u32_e32 v134, v10, v13
	v_add_u32_e32 v127, v11, v13
	v_add_u32_e32 v124, v12, v13
	v_mov_b32_e32 v3, v2
	v_mov_b32_e32 v4, v2
	v_mov_b32_e32 v5, v2
	v_mov_b32_e32 v6, v2
	v_mov_b32_e32 v7, v2
	v_mov_b32_e32 v8, v2
	v_mov_b32_e32 v9, v2
	v_mov_b32_e32 v10, v2
	v_mov_b32_e32 v11, v2
	v_mov_b32_e32 v12, v2
	v_mov_b32_e32 v13, v2
	v_mov_b32_e32 v14, v2
	v_mov_b32_e32 v15, v2
	v_mov_b32_e32 v16, v2
	v_mov_b32_e32 v17, v2
	v_mov_b32_e32 v18, v2
	v_mov_b32_e32 v19, v2
	v_mov_b32_e32 v20, v2
	v_mov_b32_e32 v21, v2
	v_mov_b32_e32 v22, v2
	v_mov_b32_e32 v23, v2
	v_mov_b32_e32 v24, v2
	v_mov_b32_e32 v25, v2
	s_waitcnt vmcnt(6)
	s_barrier

.LBB1_56:
	s_andn2_saveexec_b64 s[0:1], s[0:1]
	s_cbranch_execz .LBB1_211
	v_and_b32_e32 v122, 15, v4
	v_writelane_b32 v230, s0, 13
	v_mov_b32_e32 v107, v0
	v_ashrrev_i32_e32 v99, 31, v98
	v_cmp_lt_u32_e32 vcc, 3, v122
	v_writelane_b32 v230, s1, 14
	s_and_saveexec_b64 s[2:3], vcc
	s_cbranch_execz .LBB1_63
	v_cmp_eq_u32_e64 s[0:1], 0, v107
	s_and_b64 exec, exec, s[0:1]
	s_cbranch_execz .LBB1_62
	v_lshl_add_u64 v[252:253], v[98:99], 2, s[60:61]
	global_load_dword v254, v[252:253], off sc1
.LBB1_62:
.LBB1_63:
	s_or_b64 exec, exec, s[2:3]
	v_mul_u32_u24_e32 v121, 0xc0, v14
	v_mov_b64_e32 v[2:3], s[40:41]
	v_mad_u64_u32 v[4:5], s[0:1], v121, s56, v[2:3]
	v_bfe_i32 v3, v107, 27, 1
	v_lshlrev_b32_e32 v16, 4, v107
	v_lshrrev_b32_e32 v3, 22, v3
	v_add_u32_e32 v3, v16, v3
	v_and_b32_e32 v3, 0xfffffc00, v3
	v_sub_u32_e32 v3, v16, v3
	v_ashrrev_i32_e32 v2, 31, v107
	v_lshrrev_b32_e32 v6, 4, v3
	v_lshrrev_b32_e32 v2, 26, v2
	v_bitop3_b32 v3, v6, v3, 32 bitop3:0x6c
	v_add_u32_e32 v2, v107, v2
	v_ashrrev_i32_e32 v7, 31, v3
	v_ashrrev_i32_e32 v2, 6, v2
	v_lshrrev_b32_e32 v7, 26, v7
	v_lshlrev_b32_e32 v6, 3, v2
	v_add_u32_e32 v7, v3, v7
	v_and_b32_e32 v6, -16, v6
	v_ashrrev_i32_e32 v8, 6, v7
	v_add_u32_e32 v19, 0x2000, v16
	v_add_u32_e32 v17, v8, v6
	v_ashrrev_i32_e32 v8, 31, v19
	v_lshrrev_b32_e32 v8, 22, v8
	v_add_u32_e32 v8, v19, v8
	v_ashrrev_i32_e32 v8, 10, v8
	v_mul_i32_i24_e32 v9, 0x400, v8
	v_sub_u32_e32 v9, v19, v9
	v_lshrrev_b32_e32 v10, 4, v9
	v_bitop3_b32 v9, v10, v9, 32 bitop3:0x6c
	v_ashrrev_i32_e32 v11, 31, v9
	v_lshrrev_b32_e32 v11, 26, v11
	v_lshlrev_b32_e32 v10, 3, v8
	v_add_u32_e32 v11, v9, v11
	v_and_b32_e32 v10, -16, v10
	v_ashrrev_i32_e32 v12, 6, v11
	v_add_u32_e32 v18, v12, v10
	v_and_b32_e32 v10, 0xc0, v11
	v_and_b32_e32 v6, 0xc0, v7
	v_lshlrev_b32_e32 v8, 5, v8
	v_sub_u32_e32 v9, v9, v10
	v_lshlrev_b32_e32 v2, 5, v2
	v_sub_u32_e32 v3, v3, v6
	v_readlane_b32 s2, v230, 6
	v_and_b32_e32 v8, 32, v8
	v_ashrrev_i16_sdwa v9, v1, sext(v9) dst_sel:DWORD dst_unused:UNUSED_PAD src0_sel:DWORD src1_sel:BYTE_0
	v_and_b32_e32 v2, 32, v2
	v_ashrrev_i16_sdwa v3, v1, sext(v3) dst_sel:DWORD dst_unused:UNUSED_PAD src0_sel:DWORD src1_sel:BYTE_0
	v_mad_i64_i32 v[6:7], s[0:1], v17, s56, v[4:5]
	v_add_u32_e32 v128, s2, v16
	v_add_u32_sdwa v8, v8, sext(v9) dst_sel:DWORD dst_unused:UNUSED_PAD src0_sel:DWORD src1_sel:WORD_0
	v_add_u32_sdwa v2, v2, sext(v3) dst_sel:DWORD dst_unused:UNUSED_PAD src0_sel:DWORD src1_sel:WORD_0
	v_readfirstlane_b32 s0, v128
	v_ashrrev_i32_e32 v9, 31, v8
	v_ashrrev_i32_e32 v3, 31, v2
	s_mov_b32 m0, s0
	v_mad_i64_i32 v[10:11], s[0:1], v18, s56, v[4:5]
	v_lshlrev_b64 v[4:5], 1, v[8:9]
	v_lshlrev_b64 v[2:3], 1, v[2:3]
	v_lshl_add_u64 v[8:9], v[10:11], 0, v[4:5]
	v_add_u32_e32 v10, s2, v19
	v_lshlrev_b32_e32 v120, 8, v98
	v_lshl_add_u64 v[6:7], v[6:7], 0, v[2:3]
	v_readfirstlane_b32 s0, v10
	v_mov_b64_e32 v[20:21], s[38:39]
	v_readfirstlane_b32 s14, v122
	s_cmp_lt_u32 s14, 4
	s_cbranch_scc1 .Lpoll_done_g1
	s_and_saveexec_b64 s[100:101], s[34:35]
	s_cbranch_execz .Lpoll_w_g1
	s_waitcnt vmcnt(0)
	v_cmp_gt_i32_e64 s[16:17], 4, v254
	s_and_b64 exec, exec, s[16:17]
	s_cbranch_execz .Lpoll_w_g1
	s_mov_b32 s14, 0
	s_mov_b64 s[10:11], 0

.Lpoll_w_g1:
	s_mov_b64 exec, s[100:101]
	s_barrier
.Lpoll_done_g1:
	global_load_lds_dwordx4 v[6:7], off
	s_mov_b32 m0, s0
	v_mad_i64_i32 v[12:13], s[0:1], v120, s56, v[20:21]
	v_mad_i64_i32 v[10:11], s[0:1], v17, s56, v[12:13]
	v_add_u32_e32 v129, 0, v16
	global_load_lds_dwordx4 v[8:9], off
	v_readfirstlane_b32 s0, v129
	s_mov_b32 m0, s0
	v_mad_i64_i32 v[12:13], s[0:1], v18, s56, v[12:13]
	v_add_u32_e32 v131, 0x2000, v129
	v_mul_u32_u24_e32 v14, 0x24000, v14
	v_lshl_add_u64 v[10:11], v[10:11], 0, v[2:3]
	v_readfirstlane_b32 s0, v131
	v_lshlrev_b32_e32 v108, 1, v14
	global_load_lds_dwordx4 v[10:11], off
	s_mov_b32 m0, s0
	v_lshl_add_u64 v[14:15], s[40:41], 0, v[108:109]
	s_mov_b64 s[0:1], 0x24000
	v_lshl_add_u64 v[22:23], v[14:15], 0, s[0:1]
	v_readlane_b32 s2, v230, 7
	v_mad_i64_i32 v[24:25], s[0:1], v17, s56, v[22:23]
	s_nop 0
	v_add_u32_e32 v132, s2, v16
	v_lshl_add_u64 v[12:13], v[12:13], 0, v[4:5]
	v_readfirstlane_b32 s0, v132
	global_load_lds_dwordx4 v[12:13], off
	s_mov_b32 m0, s0
	v_mad_i64_i32 v[22:23], s[0:1], v18, s56, v[22:23]
	v_add_u32_e32 v19, s2, v19
	v_lshl_add_u64 v[24:25], v[24:25], 0, v[2:3]
	v_readfirstlane_b32 s0, v19
	v_or_b32_e32 v19, 0x80, v120
	global_load_lds_dwordx4 v[24:25], off
	v_lshl_add_u64 v[22:23], v[22:23], 0, v[4:5]
	s_mov_b32 m0, s0
	v_mad_i64_i32 v[20:21], s[0:1], v19, s56, v[20:21]
	global_load_lds_dwordx4 v[22:23], off
	v_mad_i64_i32 v[22:23], s[0:1], v17, s56, v[20:21]
	v_add_u32_e32 v134, 0x4000, v129
	v_add_u32_e32 v135, 0x6000, v129
	v_readfirstlane_b32 s0, v134
	s_mov_b32 m0, s0
	v_mad_i64_i32 v[20:21], s[0:1], v18, s56, v[20:21]
	v_lshl_add_u64 v[100:101], v[22:23], 0, v[2:3]
	v_readfirstlane_b32 s0, v135
	global_load_lds_dwordx4 v[100:101], off
	v_lshl_add_u64 v[102:103], v[20:21], 0, v[4:5]
	s_mov_b32 m0, s0
	v_and_b32_e32 v19, 0xffffff00, v107
	global_load_lds_dwordx4 v[102:103], off
	s_movk_i32 s0, 0x100
	v_cmp_eq_u32_e64 s[0:1], s0, v19
	s_and_saveexec_b64 s[2:3], s[0:1]
	s_cbranch_execz .LBB1_65
	s_barrier
.LBB1_65:
	s_or_b64 exec, exec, s[2:3]
	v_readlane_b32 s2, v230, 8
	v_mad_i64_i32 v[22:23], s[0:1], v17, s56, 0
	v_mad_i64_i32 v[18:19], s[0:1], v18, s56, 0
	v_mad_i64_i32 v[24:25], s[0:1], v120, s56, 0
	v_add_u32_e32 v137, s2, v16
	s_mov_b64 s[4:5], 0x80
	v_readfirstlane_b32 s0, v137
	v_add_u32_e32 v138, 0x2000, v137
	v_lshl_add_u64 v[6:7], v[6:7], 0, s[4:5]
	s_mov_b32 m0, s0
	v_readfirstlane_b32 s0, v138
	v_add_u32_e32 v139, 0x8000, v129
	v_mov_b32_e32 v46, 0
	v_mov_b32_e32 v47, 0
	v_mov_b32_e32 v48, 0
	v_mov_b32_e32 v49, 0
	v_mov_b32_e32 v74, 0
	v_mov_b32_e32 v75, 0
	v_mov_b32_e32 v76, 0
	v_mov_b32_e32 v77, 0
	v_mov_b32_e32 v86, 0
	v_mov_b32_e32 v87, 0
	v_mov_b32_e32 v88, 0
	v_mov_b32_e32 v89, 0
	v_mov_b32_e32 v90, 0
	v_mov_b32_e32 v91, 0
	v_mov_b32_e32 v92, 0
	v_mov_b32_e32 v93, 0
	v_mov_b32_e32 v94, 0
	v_mov_b32_e32 v95, 0
	v_mov_b32_e32 v96, 0
	v_mov_b32_e32 v97, 0
	v_mov_b32_e32 v26, 0
	v_mov_b32_e32 v27, 0
	v_mov_b32_e32 v28, 0
	v_mov_b32_e32 v29, 0
	v_mov_b32_e32 v34, 0
	v_mov_b32_e32 v35, 0
	v_mov_b32_e32 v36, 0
	v_mov_b32_e32 v37, 0
	v_mov_b32_e32 v50, 0
	v_mov_b32_e32 v51, 0
	v_mov_b32_e32 v52, 0
	v_mov_b32_e32 v53, 0
	v_mov_b32_e32 v30, 0
	v_mov_b32_e32 v31, 0
	v_mov_b32_e32 v32, 0
	v_mov_b32_e32 v33, 0
	v_mov_b32_e32 v38, 0
	v_mov_b32_e32 v39, 0
	v_mov_b32_e32 v40, 0
	v_mov_b32_e32 v41, 0
	v_mov_b32_e32 v54, 0
	v_mov_b32_e32 v55, 0
	v_mov_b32_e32 v56, 0
	v_mov_b32_e32 v57, 0
	v_mov_b32_e32 v62, 0
	v_mov_b32_e32 v63, 0
	v_mov_b32_e32 v64, 0
	v_mov_b32_e32 v65, 0
	v_mov_b32_e32 v42, 0
	v_mov_b32_e32 v43, 0
	v_mov_b32_e32 v44, 0
	v_mov_b32_e32 v45, 0
	v_mov_b32_e32 v58, 0
	v_mov_b32_e32 v59, 0
	v_mov_b32_e32 v60, 0
	v_mov_b32_e32 v61, 0
	v_mov_b32_e32 v66, 0
	v_mov_b32_e32 v67, 0
	v_mov_b32_e32 v68, 0
	v_mov_b32_e32 v69, 0
	v_mov_b32_e32 v70, 0
	v_mov_b32_e32 v71, 0
	v_mov_b32_e32 v72, 0
	v_mov_b32_e32 v73, 0
	v_mov_b32_e32 v78, 0
	v_mov_b32_e32 v79, 0
	v_mov_b32_e32 v80, 0
	v_mov_b32_e32 v81, 0
	v_mov_b32_e32 v82, 0
	v_mov_b32_e32 v83, 0
	v_mov_b32_e32 v84, 0
	v_mov_b32_e32 v85, 0
	s_waitcnt vmcnt(4)
	s_barrier
	global_load_lds_dwordx4 v[6:7], off
	v_lshl_add_u64 v[6:7], v[8:9], 0, s[4:5]
	s_mov_b32 m0, s0
	v_readfirstlane_b32 s0, v139
	v_add_u32_e32 v140, 0xa000, v129
	global_load_lds_dwordx4 v[6:7], off
	v_lshl_add_u64 v[6:7], v[10:11], 0, s[4:5]
	s_mov_b32 m0, s0
	v_readfirstlane_b32 s0, v140
	global_load_lds_dwordx4 v[6:7], off
	v_lshl_add_u64 v[6:7], v[12:13], 0, s[4:5]
	s_mov_b32 m0, s0
	s_mov_b64 s[0:1], 0x24080
	v_readlane_b32 s3, v230, 9
	global_load_lds_dwordx4 v[6:7], off
	v_lshl_add_u64 v[6:7], v[14:15], 0, s[0:1]
	v_add_u32_e32 v141, s3, v16
	v_lshl_add_u64 v[8:9], v[6:7], 0, v[22:23]
	v_readfirstlane_b32 s0, v141
	v_add_u32_e32 v142, 0x2000, v141
	v_lshl_add_u64 v[8:9], v[8:9], 0, v[2:3]
	s_mov_b32 m0, s0
	v_lshl_add_u64 v[6:7], v[6:7], 0, v[18:19]
	v_readfirstlane_b32 s0, v142
	global_load_lds_dwordx4 v[8:9], off
	v_lshl_add_u64 v[6:7], v[6:7], 0, v[4:5]
	s_mov_b32 m0, s0
	v_and_b32_e32 v125, 15, v107
	global_load_lds_dwordx4 v[6:7], off
	v_and_b32_e32 v6, 64, v107
	v_lshlrev_b32_e32 v123, 2, v107
	v_cmp_ne_u32_e64 s[0:1], 0, v6
	v_and_b32_e32 v124, 48, v107
	v_lshlrev_b32_e32 v6, 6, v125
	v_and_b32_e32 v7, 32, v123
	v_cndmask_b32_e64 v126, 0, 48, s[0:1]
	v_bitop3_b32 v6, v6, v7, v124 bitop3:0x36
	v_readlane_b32 s0, v230, 6
	v_ashrrev_i32_e32 v9, 2, v107
	v_and_b32_e32 v127, 0xffffffe0, v9
	v_add_u32_e32 v8, s0, v6
	v_readlane_b32 s0, v230, 7
	v_add_u32_e32 v10, s2, v6
	v_add_u32_e32 v11, s3, v6
	v_add_u32_e32 v9, s0, v6
	v_add_u32_e32 v13, 0, v6
	v_lshlrev_b32_e32 v6, 6, v107
	s_movk_i32 s0, 0x3c0
	v_mul_u32_u24_e32 v20, 0x600, v121
	v_mov_b32_e32 v21, v109
	v_and_or_b32 v6, v6, s0, v124
	v_lshl_add_u64 v[2:3], v[22:23], 0, v[2:3]
	v_xad_u32 v15, v6, v7, 0
	v_lshl_add_u64 v[6:7], v[2:3], 0, v[20:21]
	v_lshl_add_u64 v[4:5], v[18:19], 0, v[4:5]
	v_lshl_add_u64 v[104:105], s[40:41], 0, v[6:7]
	v_lshl_add_u64 v[6:7], v[4:5], 0, v[20:21]
	v_lshl_add_u64 v[110:111], s[40:41], 0, v[6:7]
	v_lshl_add_u64 v[6:7], v[2:3], 0, v[24:25]
	v_lshl_add_u64 v[2:3], v[2:3], 0, v[108:109]
	v_lshlrev_b32_e32 v14, 7, v127
	v_lshl_add_u64 v[116:117], s[40:41], 0, v[2:3]
	v_lshl_add_u64 v[2:3], v[4:5], 0, v[108:109]
	v_lshlrev_b32_e32 v12, 7, v126
	v_or_b32_e32 v16, 0x800, v14
	v_lshl_add_u64 v[112:113], s[38:39], 0, v[6:7]
	v_lshl_add_u64 v[6:7], v[4:5], 0, v[24:25]
	v_lshl_add_u64 v[118:119], s[40:41], 0, v[2:3]
	v_mov_b32_e32 v2, 0
	v_lshl_add_u64 v[114:115], s[38:39], 0, v[6:7]
	s_mov_b32 s2, -2
	s_mov_b64 s[0:1], 0
	v_add_u32_e32 v144, v8, v12
	v_add_u32_e32 v130, v13, v14
	v_add_u32_e32 v108, v15, v16
	v_add_u32_e32 v143, v9, v12
	v_add_u32_e32 v136, v10, v12
	v_add_u32_e32 v133, v11, v12
	v_mov_b32_e32 v3, v2
	v_mov_b32_e32 v4, v2
	v_mov_b32_e32 v5, v2
	v_mov_b32_e32 v6, v2
	v_mov_b32_e32 v7, v2
	v_mov_b32_e32 v8, v2
	v_mov_b32_e32 v9, v2
	v_mov_b32_e32 v10, v2
	v_mov_b32_e32 v11, v2
	v_mov_b32_e32 v12, v2
	v_mov_b32_e32 v13, v2
	v_mov_b32_e32 v18, v2
	v_mov_b32_e32 v19, v2
	v_mov_b32_e32 v20, v2
	v_mov_b32_e32 v21, v2
	v_mov_b32_e32 v14, v2
	v_mov_b32_e32 v15, v2
	v_mov_b32_e32 v16, v2
	v_mov_b32_e32 v17, v2
	v_mov_b32_e32 v22, v2
	v_mov_b32_e32 v23, v2
	v_mov_b32_e32 v24, v2
	v_mov_b32_e32 v25, v2
	s_waitcnt vmcnt(6)
	s_barrier
